# Z_occ8
# speedup vs baseline: 1.0564x; 1.0045x over previous
_Z11align_fusedPKfS0_PKiPf:
	s_load_dwordx8 s[4:11], s[0:1], 0x0
	s_and_b32 s3, s2, 7
	s_lshl_b32 s3, s3, 10
	s_lshr_b32 s2, s2, 3
	s_add_i32 s2, s3, s2
	s_mul_i32 s12, s2, 0x5dc0
	v_and_b32_e32 v7, 63, v0
	v_readfirstlane_b32 s13, v0
	v_lshlrev_b32_e32 v1, 4, v7
	v_mul_u32_u24_e32 v3, 12, v7
	s_mul_i32 s18, s13, 96
	s_mul_i32 s19, s13, 48
	s_mul_i32 s3, s13, 6
	s_sub_u32 s3, 0x49c, s3
	v_cmp_gt_u32_e64 s[14:15], s3, v7
	v_add_u32_e32 v2, s19, v1
	v_add_u32_e32 v3, s19, v3
	v_add_u32_e32 v4, 0x600, v3
	s_add_u32 s12, s12, s18
	s_add_u32 s12, s12, 0x800
	s_waitcnt lgkmcnt(0)
	s_add_u32 s4, s4, s12
	s_addc_u32 s5, s5, 0
	s_add_u32 s10, s10, s12
	s_addc_u32 s11, s11, 0
	s_cmp_lg_u32 s13, 0
	s_cbranch_scc1 .Lbulk_waves
	global_load_dwordx3 v[44:46], v3, s[6:7] nt
	s_load_dwordx16 s[16:31], s[8:9], 0x0
	s_load_dwordx16 s[32:47], s[8:9], 0x40
	s_load_dwordx16 s[48:63], s[8:9], 0x80
	s_waitcnt lgkmcnt(0)
	v_writelane_b32 v5, s16, 0
	v_writelane_b32 v5, s17, 1
	v_writelane_b32 v5, s18, 2
	v_writelane_b32 v5, s19, 3
	v_writelane_b32 v5, s20, 4
	v_writelane_b32 v5, s21, 5
	v_writelane_b32 v5, s22, 6
	v_writelane_b32 v5, s23, 7
	v_writelane_b32 v5, s24, 8
	v_writelane_b32 v5, s25, 9
	v_writelane_b32 v5, s26, 10
	v_writelane_b32 v5, s27, 11
	v_writelane_b32 v5, s28, 12
	v_writelane_b32 v5, s29, 13
	v_writelane_b32 v5, s30, 14
	v_writelane_b32 v5, s31, 15
	s_load_dwordx16 s[16:31], s[8:9], 0xc0
	v_writelane_b32 v5, s32, 16
	v_writelane_b32 v5, s33, 17
	v_writelane_b32 v5, s34, 18
	v_writelane_b32 v5, s35, 19
	v_writelane_b32 v5, s36, 20
	v_writelane_b32 v5, s37, 21
	v_writelane_b32 v5, s38, 22
	v_writelane_b32 v5, s39, 23
	v_writelane_b32 v5, s40, 24
	v_writelane_b32 v5, s41, 25
	v_writelane_b32 v5, s42, 26
	v_writelane_b32 v5, s43, 27
	v_writelane_b32 v5, s44, 28
	v_writelane_b32 v5, s45, 29
	v_writelane_b32 v5, s46, 30
	v_writelane_b32 v5, s47, 31
	v_writelane_b32 v5, s48, 32
	v_writelane_b32 v5, s49, 33
	v_writelane_b32 v5, s50, 34
	v_writelane_b32 v5, s51, 35
	v_writelane_b32 v5, s52, 36
	v_writelane_b32 v5, s53, 37
	v_writelane_b32 v5, s54, 38
	v_writelane_b32 v5, s55, 39
	v_writelane_b32 v5, s56, 40
	v_writelane_b32 v5, s57, 41
	v_writelane_b32 v5, s58, 42
	v_writelane_b32 v5, s59, 43
	v_writelane_b32 v5, s60, 44
	v_writelane_b32 v5, s61, 45
	v_writelane_b32 v5, s62, 46
	v_writelane_b32 v5, s63, 47
	s_waitcnt lgkmcnt(0)
	v_writelane_b32 v5, s16, 48
	v_writelane_b32 v5, s17, 49
	v_writelane_b32 v5, s18, 50
	v_writelane_b32 v5, s19, 51
	v_writelane_b32 v5, s20, 52
	v_writelane_b32 v5, s21, 53
	v_writelane_b32 v5, s22, 54
	v_writelane_b32 v5, s23, 55
	v_writelane_b32 v5, s24, 56
	v_writelane_b32 v5, s25, 57
	v_writelane_b32 v5, s26, 58
	v_writelane_b32 v5, s27, 59
	v_writelane_b32 v5, s28, 60
	v_writelane_b32 v5, s29, 61
	v_writelane_b32 v5, s30, 62
	v_writelane_b32 v5, s31, 63
	v_mul_u32_u24_e32 v5, 12, v5
	global_load_dwordx3 v[48:50], v5, s[4:5] offset:-2048 nt
	global_load_dwordx4 v[8:11], v1, s[4:5] offset:-2048 nt
	global_load_dwordx4 v[12:15], v1, s[4:5] offset:-1024 nt
	global_load_dwordx4 v[16:19], v1, s[4:5] offset:0 nt
	global_load_dwordx4 v[20:23], v1, s[4:5] offset:1024 nt
	global_load_dwordx4 v[24:27], v1, s[4:5] offset:2048 nt
	global_load_dwordx4 v[28:31], v1, s[4:5] offset:3072 nt
	s_mov_b32 s20, 0
	s_mov_b32 s21, 0x10000
	s_mov_b32 s22, 0
	s_mov_b32 s23, 0x20000
	s_mov_b32 s24, 0
	s_mov_b32 s25, 0x40000
	s_mov_b32 s26, 0
	s_mov_b32 s27, 0x80000
	s_waitcnt vmcnt(7)
	v_add_f32_dpp v52, v44, v44 quad_perm:[1,0,3,2] row_mask:0xf bank_mask:0xf
	v_add_f32_dpp v53, v45, v45 quad_perm:[1,0,3,2] row_mask:0xf bank_mask:0xf
	v_add_f32_dpp v54, v46, v46 quad_perm:[1,0,3,2] row_mask:0xf bank_mask:0xf
	v_add_f32_dpp v52, v52, v52 quad_perm:[2,3,0,1] row_mask:0xf bank_mask:0xf
	v_add_f32_dpp v53, v53, v53 quad_perm:[2,3,0,1] row_mask:0xf bank_mask:0xf
	v_add_f32_dpp v54, v54, v54 quad_perm:[2,3,0,1] row_mask:0xf bank_mask:0xf
	v_add_f32_dpp v52, v52, v52 row_half_mirror row_mask:0xf bank_mask:0xf
	v_add_f32_dpp v53, v53, v53 row_half_mirror row_mask:0xf bank_mask:0xf
	v_add_f32_dpp v54, v54, v54 row_half_mirror row_mask:0xf bank_mask:0xf
	v_add_f32_dpp v52, v52, v52 row_mirror row_mask:0xf bank_mask:0xf
	v_add_f32_dpp v53, v53, v53 row_mirror row_mask:0xf bank_mask:0xf
	v_add_f32_dpp v54, v54, v54 row_mirror row_mask:0xf bank_mask:0xf
	v_add_f32_dpp v52, v52, v52 row_bcast:15 row_mask:0xa bank_mask:0xf
	v_add_f32_dpp v53, v53, v53 row_bcast:15 row_mask:0xa bank_mask:0xf
	v_add_f32_dpp v54, v54, v54 row_bcast:15 row_mask:0xa bank_mask:0xf
	v_add_f32_dpp v52, v52, v52 row_bcast:31 row_mask:0xc bank_mask:0xf
	v_add_f32_dpp v53, v53, v53 row_bcast:31 row_mask:0xc bank_mask:0xf
	v_add_f32_dpp v54, v54, v54 row_bcast:31 row_mask:0xc bank_mask:0xf
	v_readlane_b32 s28, v52, 63
	v_readlane_b32 s29, v53, 63
	v_readlane_b32 s30, v54, 63
	v_mov_b32_e32 v52, s28
	v_mov_b32_e32 v53, s29
	v_mov_b32_e32 v54, s30
	v_fmac_f32_e32 v44, 0xbc800000, v52
	v_fmac_f32_e32 v45, 0xbc800000, v53
	v_fmac_f32_e32 v46, 0xbc800000, v54
	s_waitcnt vmcnt(6)
	v_add_f32_dpp v52, v48, v48 quad_perm:[1,0,3,2] row_mask:0xf bank_mask:0xf
	v_add_f32_dpp v53, v49, v49 quad_perm:[1,0,3,2] row_mask:0xf bank_mask:0xf
	v_add_f32_dpp v54, v50, v50 quad_perm:[1,0,3,2] row_mask:0xf bank_mask:0xf
	v_add_f32_dpp v52, v52, v52 quad_perm:[2,3,0,1] row_mask:0xf bank_mask:0xf
	v_add_f32_dpp v53, v53, v53 quad_perm:[2,3,0,1] row_mask:0xf bank_mask:0xf
	v_add_f32_dpp v54, v54, v54 quad_perm:[2,3,0,1] row_mask:0xf bank_mask:0xf
	v_add_f32_dpp v52, v52, v52 row_half_mirror row_mask:0xf bank_mask:0xf
	v_add_f32_dpp v53, v53, v53 row_half_mirror row_mask:0xf bank_mask:0xf
	v_add_f32_dpp v54, v54, v54 row_half_mirror row_mask:0xf bank_mask:0xf
	v_add_f32_dpp v52, v52, v52 row_mirror row_mask:0xf bank_mask:0xf
	v_add_f32_dpp v53, v53, v53 row_mirror row_mask:0xf bank_mask:0xf
	v_add_f32_dpp v54, v54, v54 row_mirror row_mask:0xf bank_mask:0xf
	v_add_f32_dpp v52, v52, v52 row_bcast:15 row_mask:0xa bank_mask:0xf
	v_add_f32_dpp v53, v53, v53 row_bcast:15 row_mask:0xa bank_mask:0xf
	v_add_f32_dpp v54, v54, v54 row_bcast:15 row_mask:0xa bank_mask:0xf
	v_add_f32_dpp v52, v52, v52 row_bcast:31 row_mask:0xc bank_mask:0xf
	v_add_f32_dpp v53, v53, v53 row_bcast:31 row_mask:0xc bank_mask:0xf
	v_add_f32_dpp v54, v54, v54 row_bcast:31 row_mask:0xc bank_mask:0xf
	v_readlane_b32 s32, v52, 63
	v_readlane_b32 s33, v53, 63
	v_readlane_b32 s34, v54, 63
	v_mov_b32_e32 v52, s32
	v_mov_b32_e32 v53, s33
	v_mov_b32_e32 v54, s34
	v_fmac_f32_e32 v48, 0xbc800000, v52
	v_fmac_f32_e32 v49, 0xbc800000, v53
	v_fmac_f32_e32 v50, 0xbc800000, v54
	v_mul_f32_e32 v52, v48, v44
	v_mul_f32_e32 v53, v48, v45
	v_mul_f32_e32 v54, v48, v46
	v_mul_f32_e32 v55, v49, v44
	v_mul_f32_e32 v56, v49, v45
	v_mul_f32_e32 v57, v49, v46
	v_mul_f32_e32 v58, v50, v44
	v_mul_f32_e32 v59, v50, v45
	v_mul_f32_e32 v60, v50, v46
	v_add_f32_dpp v52, v52, v52 quad_perm:[1,0,3,2] row_mask:0xf bank_mask:0xf
	v_add_f32_dpp v53, v53, v53 quad_perm:[1,0,3,2] row_mask:0xf bank_mask:0xf
	v_add_f32_dpp v54, v54, v54 quad_perm:[1,0,3,2] row_mask:0xf bank_mask:0xf
	v_add_f32_dpp v55, v55, v55 quad_perm:[1,0,3,2] row_mask:0xf bank_mask:0xf
	v_add_f32_dpp v56, v56, v56 quad_perm:[1,0,3,2] row_mask:0xf bank_mask:0xf
	v_add_f32_dpp v57, v57, v57 quad_perm:[1,0,3,2] row_mask:0xf bank_mask:0xf
	v_add_f32_dpp v58, v58, v58 quad_perm:[1,0,3,2] row_mask:0xf bank_mask:0xf
	v_add_f32_dpp v59, v59, v59 quad_perm:[1,0,3,2] row_mask:0xf bank_mask:0xf
	v_add_f32_dpp v60, v60, v60 quad_perm:[1,0,3,2] row_mask:0xf bank_mask:0xf
	v_add_f32_dpp v52, v52, v52 quad_perm:[2,3,0,1] row_mask:0xf bank_mask:0xf
	v_add_f32_dpp v53, v53, v53 quad_perm:[2,3,0,1] row_mask:0xf bank_mask:0xf
	v_add_f32_dpp v54, v54, v54 quad_perm:[2,3,0,1] row_mask:0xf bank_mask:0xf
	v_add_f32_dpp v55, v55, v55 quad_perm:[2,3,0,1] row_mask:0xf bank_mask:0xf
	v_add_f32_dpp v56, v56, v56 quad_perm:[2,3,0,1] row_mask:0xf bank_mask:0xf
	v_add_f32_dpp v57, v57, v57 quad_perm:[2,3,0,1] row_mask:0xf bank_mask:0xf
	v_add_f32_dpp v58, v58, v58 quad_perm:[2,3,0,1] row_mask:0xf bank_mask:0xf
	v_add_f32_dpp v59, v59, v59 quad_perm:[2,3,0,1] row_mask:0xf bank_mask:0xf
	v_add_f32_dpp v60, v60, v60 quad_perm:[2,3,0,1] row_mask:0xf bank_mask:0xf
	v_add_f32_dpp v52, v52, v52 row_half_mirror row_mask:0xf bank_mask:0xf
	v_add_f32_dpp v53, v53, v53 row_half_mirror row_mask:0xf bank_mask:0xf
	v_add_f32_dpp v54, v54, v54 row_half_mirror row_mask:0xf bank_mask:0xf
	v_add_f32_dpp v55, v55, v55 row_half_mirror row_mask:0xf bank_mask:0xf
	v_add_f32_dpp v56, v56, v56 row_half_mirror row_mask:0xf bank_mask:0xf
	v_add_f32_dpp v57, v57, v57 row_half_mirror row_mask:0xf bank_mask:0xf
	v_add_f32_dpp v58, v58, v58 row_half_mirror row_mask:0xf bank_mask:0xf
	v_add_f32_dpp v59, v59, v59 row_half_mirror row_mask:0xf bank_mask:0xf
	v_add_f32_dpp v60, v60, v60 row_half_mirror row_mask:0xf bank_mask:0xf
	v_add_f32_dpp v52, v52, v52 row_mirror row_mask:0xf bank_mask:0xf
	v_add_f32_dpp v53, v53, v53 row_mirror row_mask:0xf bank_mask:0xf
	v_add_f32_dpp v54, v54, v54 row_mirror row_mask:0xf bank_mask:0xf
	v_add_f32_dpp v55, v55, v55 row_mirror row_mask:0xf bank_mask:0xf
	v_add_f32_dpp v56, v56, v56 row_mirror row_mask:0xf bank_mask:0xf
	v_add_f32_dpp v57, v57, v57 row_mirror row_mask:0xf bank_mask:0xf
	v_add_f32_dpp v58, v58, v58 row_mirror row_mask:0xf bank_mask:0xf
	v_add_f32_dpp v59, v59, v59 row_mirror row_mask:0xf bank_mask:0xf
	v_add_f32_dpp v60, v60, v60 row_mirror row_mask:0xf bank_mask:0xf
	v_add_f32_dpp v52, v52, v52 row_bcast:15 row_mask:0xa bank_mask:0xf
	v_add_f32_dpp v53, v53, v53 row_bcast:15 row_mask:0xa bank_mask:0xf
	v_add_f32_dpp v54, v54, v54 row_bcast:15 row_mask:0xa bank_mask:0xf
	v_add_f32_dpp v55, v55, v55 row_bcast:15 row_mask:0xa bank_mask:0xf
	v_add_f32_dpp v56, v56, v56 row_bcast:15 row_mask:0xa bank_mask:0xf
	v_add_f32_dpp v57, v57, v57 row_bcast:15 row_mask:0xa bank_mask:0xf
	v_add_f32_dpp v58, v58, v58 row_bcast:15 row_mask:0xa bank_mask:0xf
	v_add_f32_dpp v59, v59, v59 row_bcast:15 row_mask:0xa bank_mask:0xf
	v_add_f32_dpp v60, v60, v60 row_bcast:15 row_mask:0xa bank_mask:0xf
	v_add_f32_dpp v52, v52, v52 row_bcast:31 row_mask:0xc bank_mask:0xf
	v_add_f32_dpp v53, v53, v53 row_bcast:31 row_mask:0xc bank_mask:0xf
	v_add_f32_dpp v54, v54, v54 row_bcast:31 row_mask:0xc bank_mask:0xf
	v_add_f32_dpp v55, v55, v55 row_bcast:31 row_mask:0xc bank_mask:0xf
	v_add_f32_dpp v56, v56, v56 row_bcast:31 row_mask:0xc bank_mask:0xf
	v_add_f32_dpp v57, v57, v57 row_bcast:31 row_mask:0xc bank_mask:0xf
	v_add_f32_dpp v58, v58, v58 row_bcast:31 row_mask:0xc bank_mask:0xf
	v_add_f32_dpp v59, v59, v59 row_bcast:31 row_mask:0xc bank_mask:0xf
	v_add_f32_dpp v60, v60, v60 row_bcast:31 row_mask:0xc bank_mask:0xf
	v_cndmask_b32_e64 v52, v52, v55, s[22:23]
	v_cndmask_b32_e64 v53, v53, v56, s[22:23]
	v_cndmask_b32_e64 v54, v54, v57, s[22:23]
	v_cndmask_b32_e64 v52, v52, v58, s[24:25]
	v_cndmask_b32_e64 v53, v53, v59, s[24:25]
	v_cndmask_b32_e64 v54, v54, v60, s[24:25]
	v_cndmask_b32_e64 v52, v52, 0, s[26:27]
	v_cndmask_b32_e64 v53, v53, 0, s[26:27]
	v_cndmask_b32_e64 v54, v54, 0, s[26:27]
	v_cndmask_b32_e64 v40, 0, 1.0, s[20:21]
	v_cndmask_b32_e64 v41, 0, 1.0, s[22:23]
	v_cndmask_b32_e64 v42, 0, 1.0, s[24:25]
	v_mul_f32_e32 v55, v52, v52
	v_mul_f32_e32 v56, v53, v53
	v_mul_f32_e32 v57, v52, v53
	v_add_f32_dpp v55, v55, v55 quad_perm:[1,0,3,2] row_mask:0xf bank_mask:0xf
	v_add_f32_dpp v56, v56, v56 quad_perm:[1,0,3,2] row_mask:0xf bank_mask:0xf
	v_add_f32_dpp v57, v57, v57 quad_perm:[1,0,3,2] row_mask:0xf bank_mask:0xf
	v_add_f32_dpp v55, v55, v55 quad_perm:[2,3,0,1] row_mask:0xf bank_mask:0xf
	v_add_f32_dpp v56, v56, v56 quad_perm:[2,3,0,1] row_mask:0xf bank_mask:0xf
	v_add_f32_dpp v57, v57, v57 quad_perm:[2,3,0,1] row_mask:0xf bank_mask:0xf
	v_sub_f32_e32 v60, v56, v55
	v_mul_f32_e32 v58, v57, v57
	v_cmp_gt_f32_e32 vcc, 0, v60
	v_mul_f32_e32 v59, v60, v60
	v_fmac_f32_e32 v59, 4.0, v58
	v_sqrt_f32_e32 v59, v59
	s_nop 0
	v_add_f32_e64 v59, |v60|, v59
	v_add_f32_e32 v59, 0x0da24260, v59
	v_rcp_f32_e32 v59, v59
	v_add_f32_e32 v58, v57, v57
	v_mul_f32_e32 v59, v58, v59
	v_cndmask_b32_e64 v59, v59, -v59, vcc
	v_fma_f32 v58, v59, v59, 1.0
	v_rsq_f32_e32 v61, v58
	s_nop 0
	v_mul_f32_e32 v62, v61, v59
	v_mul_f32_e32 v55, v62, v53
	v_mul_f32_e32 v56, v62, v52
	v_fma_f32 v52, v61, v52, -v55
	v_fma_f32 v53, v61, v53, v56
	v_mul_f32_e32 v55, v52, v52
	v_mul_f32_e32 v56, v54, v54
	v_mul_f32_e32 v57, v52, v54
	v_add_f32_dpp v55, v55, v55 quad_perm:[1,0,3,2] row_mask:0xf bank_mask:0xf
	v_add_f32_dpp v56, v56, v56 quad_perm:[1,0,3,2] row_mask:0xf bank_mask:0xf
	v_add_f32_dpp v57, v57, v57 quad_perm:[1,0,3,2] row_mask:0xf bank_mask:0xf
	v_add_f32_dpp v55, v55, v55 quad_perm:[2,3,0,1] row_mask:0xf bank_mask:0xf
	v_add_f32_dpp v56, v56, v56 quad_perm:[2,3,0,1] row_mask:0xf bank_mask:0xf
	v_add_f32_dpp v57, v57, v57 quad_perm:[2,3,0,1] row_mask:0xf bank_mask:0xf
	v_sub_f32_e32 v60, v56, v55
	v_mul_f32_e32 v58, v57, v57
	v_cmp_gt_f32_e32 vcc, 0, v60
	v_mul_f32_e32 v59, v60, v60
	v_fmac_f32_e32 v59, 4.0, v58
	v_sqrt_f32_e32 v59, v59
	v_mul_f32_e32 v63, v62, v41
	v_mul_f32_e32 v43, v62, v40
	v_fma_f32 v40, v61, v40, -v63
	v_fma_f32 v41, v61, v41, v43
	v_add_f32_e64 v59, |v60|, v59
	v_add_f32_e32 v59, 0x0da24260, v59
	v_rcp_f32_e32 v59, v59
	v_add_f32_e32 v58, v57, v57
	v_mul_f32_e32 v59, v58, v59
	v_cndmask_b32_e64 v59, v59, -v59, vcc
	v_fma_f32 v58, v59, v59, 1.0
	v_rsq_f32_e32 v61, v58
	s_nop 0
	v_mul_f32_e32 v62, v61, v59
	v_mul_f32_e32 v55, v62, v54
	v_mul_f32_e32 v56, v62, v52
	v_fma_f32 v52, v61, v52, -v55
	v_fma_f32 v54, v61, v54, v56
	v_mul_f32_e32 v55, v53, v53
	v_mul_f32_e32 v56, v54, v54
	v_mul_f32_e32 v57, v53, v54
	v_add_f32_dpp v55, v55, v55 quad_perm:[1,0,3,2] row_mask:0xf bank_mask:0xf
	v_add_f32_dpp v56, v56, v56 quad_perm:[1,0,3,2] row_mask:0xf bank_mask:0xf
	v_add_f32_dpp v57, v57, v57 quad_perm:[1,0,3,2] row_mask:0xf bank_mask:0xf
	v_add_f32_dpp v55, v55, v55 quad_perm:[2,3,0,1] row_mask:0xf bank_mask:0xf
	v_add_f32_dpp v56, v56, v56 quad_perm:[2,3,0,1] row_mask:0xf bank_mask:0xf
	v_add_f32_dpp v57, v57, v57 quad_perm:[2,3,0,1] row_mask:0xf bank_mask:0xf
	v_sub_f32_e32 v60, v56, v55
	v_mul_f32_e32 v58, v57, v57
	v_cmp_gt_f32_e32 vcc, 0, v60
	v_mul_f32_e32 v59, v60, v60
	v_fmac_f32_e32 v59, 4.0, v58
	v_sqrt_f32_e32 v59, v59
	v_mul_f32_e32 v63, v62, v42
	v_mul_f32_e32 v43, v62, v40
	v_fma_f32 v40, v61, v40, -v63
	v_fma_f32 v42, v61, v42, v43
	v_add_f32_e64 v59, |v60|, v59
	v_add_f32_e32 v59, 0x0da24260, v59
	v_rcp_f32_e32 v59, v59
	v_add_f32_e32 v58, v57, v57
	v_mul_f32_e32 v59, v58, v59
	v_cndmask_b32_e64 v59, v59, -v59, vcc
	v_fma_f32 v58, v59, v59, 1.0
	v_rsq_f32_e32 v61, v58
	s_nop 0
	v_mul_f32_e32 v62, v61, v59
	v_mul_f32_e32 v55, v62, v54
	v_mul_f32_e32 v56, v62, v53
	v_fma_f32 v53, v61, v53, -v55
	v_fma_f32 v54, v61, v54, v56
	v_mul_f32_e32 v55, v52, v52
	v_mul_f32_e32 v56, v53, v53
	v_mul_f32_e32 v57, v52, v53
	v_add_f32_dpp v55, v55, v55 quad_perm:[1,0,3,2] row_mask:0xf bank_mask:0xf
	v_add_f32_dpp v56, v56, v56 quad_perm:[1,0,3,2] row_mask:0xf bank_mask:0xf
	v_add_f32_dpp v57, v57, v57 quad_perm:[1,0,3,2] row_mask:0xf bank_mask:0xf
	v_add_f32_dpp v55, v55, v55 quad_perm:[2,3,0,1] row_mask:0xf bank_mask:0xf
	v_add_f32_dpp v56, v56, v56 quad_perm:[2,3,0,1] row_mask:0xf bank_mask:0xf
	v_add_f32_dpp v57, v57, v57 quad_perm:[2,3,0,1] row_mask:0xf bank_mask:0xf
	v_sub_f32_e32 v60, v56, v55
	v_mul_f32_e32 v58, v57, v57
	v_cmp_gt_f32_e32 vcc, 0, v60
	v_mul_f32_e32 v59, v60, v60
	v_fmac_f32_e32 v59, 4.0, v58
	v_sqrt_f32_e32 v59, v59
	v_mul_f32_e32 v63, v62, v42
	v_mul_f32_e32 v43, v62, v41
	v_fma_f32 v41, v61, v41, -v63
	v_fma_f32 v42, v61, v42, v43
	v_add_f32_e64 v59, |v60|, v59
	v_add_f32_e32 v59, 0x0da24260, v59
	v_rcp_f32_e32 v59, v59
	v_add_f32_e32 v58, v57, v57
	v_mul_f32_e32 v59, v58, v59
	v_cndmask_b32_e64 v59, v59, -v59, vcc
	v_fma_f32 v58, v59, v59, 1.0
	v_rsq_f32_e32 v61, v58
	s_nop 0
	v_mul_f32_e32 v62, v61, v59
	v_mul_f32_e32 v55, v62, v53
	v_mul_f32_e32 v56, v62, v52
	v_fma_f32 v52, v61, v52, -v55
	v_fma_f32 v53, v61, v53, v56
	v_mul_f32_e32 v55, v52, v52
	v_mul_f32_e32 v56, v54, v54
	v_mul_f32_e32 v57, v52, v54
	v_add_f32_dpp v55, v55, v55 quad_perm:[1,0,3,2] row_mask:0xf bank_mask:0xf
	v_add_f32_dpp v56, v56, v56 quad_perm:[1,0,3,2] row_mask:0xf bank_mask:0xf
	v_add_f32_dpp v57, v57, v57 quad_perm:[1,0,3,2] row_mask:0xf bank_mask:0xf
	v_add_f32_dpp v55, v55, v55 quad_perm:[2,3,0,1] row_mask:0xf bank_mask:0xf
	v_add_f32_dpp v56, v56, v56 quad_perm:[2,3,0,1] row_mask:0xf bank_mask:0xf
	v_add_f32_dpp v57, v57, v57 quad_perm:[2,3,0,1] row_mask:0xf bank_mask:0xf
	v_sub_f32_e32 v60, v56, v55
	v_mul_f32_e32 v58, v57, v57
	v_cmp_gt_f32_e32 vcc, 0, v60
	v_mul_f32_e32 v59, v60, v60
	v_fmac_f32_e32 v59, 4.0, v58
	v_sqrt_f32_e32 v59, v59
	v_mul_f32_e32 v63, v62, v41
	v_mul_f32_e32 v43, v62, v40
	v_fma_f32 v40, v61, v40, -v63
	v_fma_f32 v41, v61, v41, v43
	v_add_f32_e64 v59, |v60|, v59
	v_add_f32_e32 v59, 0x0da24260, v59
	v_rcp_f32_e32 v59, v59
	v_add_f32_e32 v58, v57, v57
	v_mul_f32_e32 v59, v58, v59
	v_cndmask_b32_e64 v59, v59, -v59, vcc
	v_fma_f32 v58, v59, v59, 1.0
	v_rsq_f32_e32 v61, v58
	s_nop 0
	v_mul_f32_e32 v62, v61, v59
	v_mul_f32_e32 v55, v62, v54
	v_mul_f32_e32 v56, v62, v52
	v_fma_f32 v52, v61, v52, -v55
	v_fma_f32 v54, v61, v54, v56
	v_mul_f32_e32 v55, v53, v53
	v_mul_f32_e32 v56, v54, v54
	v_mul_f32_e32 v57, v53, v54
	v_add_f32_dpp v55, v55, v55 quad_perm:[1,0,3,2] row_mask:0xf bank_mask:0xf
	v_add_f32_dpp v56, v56, v56 quad_perm:[1,0,3,2] row_mask:0xf bank_mask:0xf
	v_add_f32_dpp v57, v57, v57 quad_perm:[1,0,3,2] row_mask:0xf bank_mask:0xf
	v_add_f32_dpp v55, v55, v55 quad_perm:[2,3,0,1] row_mask:0xf bank_mask:0xf
	v_add_f32_dpp v56, v56, v56 quad_perm:[2,3,0,1] row_mask:0xf bank_mask:0xf
	v_add_f32_dpp v57, v57, v57 quad_perm:[2,3,0,1] row_mask:0xf bank_mask:0xf
	v_sub_f32_e32 v60, v56, v55
	v_mul_f32_e32 v58, v57, v57
	v_cmp_gt_f32_e32 vcc, 0, v60
	v_mul_f32_e32 v59, v60, v60
	v_fmac_f32_e32 v59, 4.0, v58
	v_sqrt_f32_e32 v59, v59
	v_mul_f32_e32 v63, v62, v42
	v_mul_f32_e32 v43, v62, v40
	v_fma_f32 v40, v61, v40, -v63
	v_fma_f32 v42, v61, v42, v43
	v_add_f32_e64 v59, |v60|, v59
	v_add_f32_e32 v59, 0x0da24260, v59
	v_rcp_f32_e32 v59, v59
	v_add_f32_e32 v58, v57, v57
	v_mul_f32_e32 v59, v58, v59
	v_cndmask_b32_e64 v59, v59, -v59, vcc
	v_fma_f32 v58, v59, v59, 1.0
	v_rsq_f32_e32 v61, v58
	s_nop 0
	v_mul_f32_e32 v62, v61, v59
	v_mul_f32_e32 v55, v62, v54
	v_mul_f32_e32 v56, v62, v53
	v_fma_f32 v53, v61, v53, -v55
	v_fma_f32 v54, v61, v54, v56
	v_mul_f32_e32 v55, v52, v52
	v_mul_f32_e32 v56, v53, v53
	v_mul_f32_e32 v57, v52, v53
	v_add_f32_dpp v55, v55, v55 quad_perm:[1,0,3,2] row_mask:0xf bank_mask:0xf
	v_add_f32_dpp v56, v56, v56 quad_perm:[1,0,3,2] row_mask:0xf bank_mask:0xf
	v_add_f32_dpp v57, v57, v57 quad_perm:[1,0,3,2] row_mask:0xf bank_mask:0xf
	v_add_f32_dpp v55, v55, v55 quad_perm:[2,3,0,1] row_mask:0xf bank_mask:0xf
	v_add_f32_dpp v56, v56, v56 quad_perm:[2,3,0,1] row_mask:0xf bank_mask:0xf
	v_add_f32_dpp v57, v57, v57 quad_perm:[2,3,0,1] row_mask:0xf bank_mask:0xf
	v_sub_f32_e32 v60, v56, v55
	v_mul_f32_e32 v58, v57, v57
	v_cmp_gt_f32_e32 vcc, 0, v60
	v_mul_f32_e32 v59, v60, v60
	v_fmac_f32_e32 v59, 4.0, v58
	v_sqrt_f32_e32 v59, v59
	v_mul_f32_e32 v63, v62, v42
	v_mul_f32_e32 v43, v62, v41
	v_fma_f32 v41, v61, v41, -v63
	v_fma_f32 v42, v61, v42, v43
	v_add_f32_e64 v59, |v60|, v59
	v_add_f32_e32 v59, 0x0da24260, v59
	v_rcp_f32_e32 v59, v59
	v_add_f32_e32 v58, v57, v57
	v_mul_f32_e32 v59, v58, v59
	v_cndmask_b32_e64 v59, v59, -v59, vcc
	v_fma_f32 v58, v59, v59, 1.0
	v_rsq_f32_e32 v61, v58
	s_nop 0
	v_mul_f32_e32 v62, v61, v59
	v_mul_f32_e32 v55, v62, v53
	v_mul_f32_e32 v56, v62, v52
	v_fma_f32 v52, v61, v52, -v55
	v_fma_f32 v53, v61, v53, v56
	v_mul_f32_e32 v55, v52, v52
	v_mul_f32_e32 v56, v54, v54
	v_mul_f32_e32 v57, v52, v54
	v_add_f32_dpp v55, v55, v55 quad_perm:[1,0,3,2] row_mask:0xf bank_mask:0xf
	v_add_f32_dpp v56, v56, v56 quad_perm:[1,0,3,2] row_mask:0xf bank_mask:0xf
	v_add_f32_dpp v57, v57, v57 quad_perm:[1,0,3,2] row_mask:0xf bank_mask:0xf
	v_add_f32_dpp v55, v55, v55 quad_perm:[2,3,0,1] row_mask:0xf bank_mask:0xf
	v_add_f32_dpp v56, v56, v56 quad_perm:[2,3,0,1] row_mask:0xf bank_mask:0xf
	v_add_f32_dpp v57, v57, v57 quad_perm:[2,3,0,1] row_mask:0xf bank_mask:0xf
	v_sub_f32_e32 v60, v56, v55
	v_mul_f32_e32 v58, v57, v57
	v_cmp_gt_f32_e32 vcc, 0, v60
	v_mul_f32_e32 v59, v60, v60
	v_fmac_f32_e32 v59, 4.0, v58
	v_sqrt_f32_e32 v59, v59
	v_mul_f32_e32 v63, v62, v41
	v_mul_f32_e32 v43, v62, v40
	v_fma_f32 v40, v61, v40, -v63
	v_fma_f32 v41, v61, v41, v43
	v_add_f32_e64 v59, |v60|, v59
	v_add_f32_e32 v59, 0x0da24260, v59
	v_rcp_f32_e32 v59, v59
	v_add_f32_e32 v58, v57, v57
	v_mul_f32_e32 v59, v58, v59
	v_cndmask_b32_e64 v59, v59, -v59, vcc
	v_fma_f32 v58, v59, v59, 1.0
	v_rsq_f32_e32 v61, v58
	s_nop 0
	v_mul_f32_e32 v62, v61, v59
	v_mul_f32_e32 v55, v62, v54
	v_mul_f32_e32 v56, v62, v52
	v_fma_f32 v52, v61, v52, -v55
	v_fma_f32 v54, v61, v54, v56
	v_mul_f32_e32 v55, v53, v53
	v_mul_f32_e32 v56, v54, v54
	v_mul_f32_e32 v57, v53, v54
	v_add_f32_dpp v55, v55, v55 quad_perm:[1,0,3,2] row_mask:0xf bank_mask:0xf
	v_add_f32_dpp v56, v56, v56 quad_perm:[1,0,3,2] row_mask:0xf bank_mask:0xf
	v_add_f32_dpp v57, v57, v57 quad_perm:[1,0,3,2] row_mask:0xf bank_mask:0xf
	v_add_f32_dpp v55, v55, v55 quad_perm:[2,3,0,1] row_mask:0xf bank_mask:0xf
	v_add_f32_dpp v56, v56, v56 quad_perm:[2,3,0,1] row_mask:0xf bank_mask:0xf
	v_add_f32_dpp v57, v57, v57 quad_perm:[2,3,0,1] row_mask:0xf bank_mask:0xf
	v_sub_f32_e32 v60, v56, v55
	v_mul_f32_e32 v58, v57, v57
	v_cmp_gt_f32_e32 vcc, 0, v60
	v_mul_f32_e32 v59, v60, v60
	v_fmac_f32_e32 v59, 4.0, v58
	v_sqrt_f32_e32 v59, v59
	v_mul_f32_e32 v63, v62, v42
	v_mul_f32_e32 v43, v62, v40
	v_fma_f32 v40, v61, v40, -v63
	v_fma_f32 v42, v61, v42, v43
	v_add_f32_e64 v59, |v60|, v59
	v_add_f32_e32 v59, 0x0da24260, v59
	v_rcp_f32_e32 v59, v59
	v_add_f32_e32 v58, v57, v57
	v_mul_f32_e32 v59, v58, v59
	v_cndmask_b32_e64 v59, v59, -v59, vcc
	v_fma_f32 v58, v59, v59, 1.0
	v_rsq_f32_e32 v61, v58
	s_nop 0
	v_mul_f32_e32 v62, v61, v59
	v_mul_f32_e32 v55, v62, v54
	v_mul_f32_e32 v56, v62, v53
	v_fma_f32 v53, v61, v53, -v55
	v_fma_f32 v54, v61, v54, v56
	v_mul_f32_e32 v55, v52, v52
	v_mul_f32_e32 v56, v53, v53
	v_mul_f32_e32 v57, v52, v53
	v_add_f32_dpp v55, v55, v55 quad_perm:[1,0,3,2] row_mask:0xf bank_mask:0xf
	v_add_f32_dpp v56, v56, v56 quad_perm:[1,0,3,2] row_mask:0xf bank_mask:0xf
	v_add_f32_dpp v57, v57, v57 quad_perm:[1,0,3,2] row_mask:0xf bank_mask:0xf
	v_add_f32_dpp v55, v55, v55 quad_perm:[2,3,0,1] row_mask:0xf bank_mask:0xf
	v_add_f32_dpp v56, v56, v56 quad_perm:[2,3,0,1] row_mask:0xf bank_mask:0xf
	v_add_f32_dpp v57, v57, v57 quad_perm:[2,3,0,1] row_mask:0xf bank_mask:0xf
	v_sub_f32_e32 v60, v56, v55
	v_mul_f32_e32 v58, v57, v57
	v_cmp_gt_f32_e32 vcc, 0, v60
	v_mul_f32_e32 v59, v60, v60
	v_fmac_f32_e32 v59, 4.0, v58
	v_sqrt_f32_e32 v59, v59
	v_mul_f32_e32 v63, v62, v42
	v_mul_f32_e32 v43, v62, v41
	v_fma_f32 v41, v61, v41, -v63
	v_fma_f32 v42, v61, v42, v43
	v_add_f32_e64 v59, |v60|, v59
	v_add_f32_e32 v59, 0x0da24260, v59
	v_rcp_f32_e32 v59, v59
	v_add_f32_e32 v58, v57, v57
	v_mul_f32_e32 v59, v58, v59
	v_cndmask_b32_e64 v59, v59, -v59, vcc
	v_fma_f32 v58, v59, v59, 1.0
	v_rsq_f32_e32 v61, v58
	s_nop 0
	v_mul_f32_e32 v62, v61, v59
	v_mul_f32_e32 v55, v62, v53
	v_mul_f32_e32 v56, v62, v52
	v_fma_f32 v52, v61, v52, -v55
	v_fma_f32 v53, v61, v53, v56
	v_mul_f32_e32 v55, v52, v52
	v_mul_f32_e32 v56, v54, v54
	v_mul_f32_e32 v57, v52, v54
	v_add_f32_dpp v55, v55, v55 quad_perm:[1,0,3,2] row_mask:0xf bank_mask:0xf
	v_add_f32_dpp v56, v56, v56 quad_perm:[1,0,3,2] row_mask:0xf bank_mask:0xf
	v_add_f32_dpp v57, v57, v57 quad_perm:[1,0,3,2] row_mask:0xf bank_mask:0xf
	v_add_f32_dpp v55, v55, v55 quad_perm:[2,3,0,1] row_mask:0xf bank_mask:0xf
	v_add_f32_dpp v56, v56, v56 quad_perm:[2,3,0,1] row_mask:0xf bank_mask:0xf
	v_add_f32_dpp v57, v57, v57 quad_perm:[2,3,0,1] row_mask:0xf bank_mask:0xf
	v_sub_f32_e32 v60, v56, v55
	v_mul_f32_e32 v58, v57, v57
	v_cmp_gt_f32_e32 vcc, 0, v60
	v_mul_f32_e32 v59, v60, v60
	v_fmac_f32_e32 v59, 4.0, v58
	v_sqrt_f32_e32 v59, v59
	v_mul_f32_e32 v63, v62, v41
	v_mul_f32_e32 v43, v62, v40
	v_fma_f32 v40, v61, v40, -v63
	v_fma_f32 v41, v61, v41, v43
	v_add_f32_e64 v59, |v60|, v59
	v_add_f32_e32 v59, 0x0da24260, v59
	v_rcp_f32_e32 v59, v59
	v_add_f32_e32 v58, v57, v57
	v_mul_f32_e32 v59, v58, v59
	v_cndmask_b32_e64 v59, v59, -v59, vcc
	v_fma_f32 v58, v59, v59, 1.0
	v_rsq_f32_e32 v61, v58
	s_nop 0
	v_mul_f32_e32 v62, v61, v59
	v_mul_f32_e32 v55, v62, v54
	v_mul_f32_e32 v56, v62, v52
	v_fma_f32 v52, v61, v52, -v55
	v_fma_f32 v54, v61, v54, v56
	v_mul_f32_e32 v55, v53, v53
	v_mul_f32_e32 v56, v54, v54
	v_mul_f32_e32 v57, v53, v54
	v_add_f32_dpp v55, v55, v55 quad_perm:[1,0,3,2] row_mask:0xf bank_mask:0xf
	v_add_f32_dpp v56, v56, v56 quad_perm:[1,0,3,2] row_mask:0xf bank_mask:0xf
	v_add_f32_dpp v57, v57, v57 quad_perm:[1,0,3,2] row_mask:0xf bank_mask:0xf
	v_add_f32_dpp v55, v55, v55 quad_perm:[2,3,0,1] row_mask:0xf bank_mask:0xf
	v_add_f32_dpp v56, v56, v56 quad_perm:[2,3,0,1] row_mask:0xf bank_mask:0xf
	v_add_f32_dpp v57, v57, v57 quad_perm:[2,3,0,1] row_mask:0xf bank_mask:0xf
	v_sub_f32_e32 v60, v56, v55
	v_mul_f32_e32 v58, v57, v57
	v_cmp_gt_f32_e32 vcc, 0, v60
	v_mul_f32_e32 v59, v60, v60
	v_fmac_f32_e32 v59, 4.0, v58
	v_sqrt_f32_e32 v59, v59
	v_mul_f32_e32 v63, v62, v42
	v_mul_f32_e32 v43, v62, v40
	v_fma_f32 v40, v61, v40, -v63
	v_fma_f32 v42, v61, v42, v43
	v_add_f32_e64 v59, |v60|, v59
	v_add_f32_e32 v59, 0x0da24260, v59
	v_rcp_f32_e32 v59, v59
	v_add_f32_e32 v58, v57, v57
	v_mul_f32_e32 v59, v58, v59
	v_cndmask_b32_e64 v59, v59, -v59, vcc
	v_fma_f32 v58, v59, v59, 1.0
	v_rsq_f32_e32 v61, v58
	s_nop 0
	v_mul_f32_e32 v62, v61, v59
	v_mul_f32_e32 v55, v62, v54
	v_mul_f32_e32 v56, v62, v53
	v_fma_f32 v53, v61, v53, -v55
	v_fma_f32 v54, v61, v54, v56
	v_mul_f32_e32 v63, v62, v42
	v_mul_f32_e32 v43, v62, v41
	v_fma_f32 v41, v61, v41, -v63
	v_fma_f32 v42, v61, v42, v43
	v_mul_f32_e32 v55, v52, v52
	v_mul_f32_e32 v56, v53, v53
	v_mul_f32_e32 v57, v54, v54
	v_add_f32_dpp v55, v55, v55 quad_perm:[1,0,3,2] row_mask:0xf bank_mask:0xf
	v_add_f32_dpp v56, v56, v56 quad_perm:[1,0,3,2] row_mask:0xf bank_mask:0xf
	v_add_f32_dpp v57, v57, v57 quad_perm:[1,0,3,2] row_mask:0xf bank_mask:0xf
	v_add_f32_dpp v55, v55, v55 quad_perm:[2,3,0,1] row_mask:0xf bank_mask:0xf
	v_add_f32_dpp v56, v56, v56 quad_perm:[2,3,0,1] row_mask:0xf bank_mask:0xf
	v_add_f32_dpp v57, v57, v57 quad_perm:[2,3,0,1] row_mask:0xf bank_mask:0xf
	v_cmp_le_f32_e64 s[28:29], v55, v56
	v_cmp_le_f32_e64 s[30:31], v55, v57
	v_cmp_lt_f32_e32 vcc, v57, v56
	s_and_b64 s[28:29], s[28:29], s[30:31]
	s_andn2_b64 s[30:31], vcc, s[28:29]
	v_cndmask_b32_e64 v44, v52, v53, s[28:29]
	v_cndmask_b32_e64 v45, v54, v53, s[30:31]
	v_cndmask_b32_e64 v46, v40, v41, s[28:29]
	v_cndmask_b32_e64 v47, v42, v41, s[30:31]
	v_mul_f32_e32 v58, v44, v44
	s_nop 1
	v_add_f32_dpp v58, v58, v58 quad_perm:[1,0,3,2] row_mask:0xf bank_mask:0xf
	s_nop 1
	v_add_f32_dpp v58, v58, v58 quad_perm:[2,3,0,1] row_mask:0xf bank_mask:0xf
	v_max_f32_e32 v58, 0x3aa2425, v58
	v_rsq_f32_e32 v58, v58
	s_nop 0
	v_mul_f32_e32 v48, v44, v58
	v_mul_f32_e32 v59, v48, v45
	s_nop 1
	v_add_f32_dpp v59, v59, v59 quad_perm:[1,0,3,2] row_mask:0xf bank_mask:0xf
	s_nop 1
	v_add_f32_dpp v59, v59, v59 quad_perm:[2,3,0,1] row_mask:0xf bank_mask:0xf
	v_fma_f32 v49, -v59, v48, v45
	v_mul_f32_e32 v58, v49, v49
	s_nop 1
	v_add_f32_dpp v58, v58, v58 quad_perm:[1,0,3,2] row_mask:0xf bank_mask:0xf
	s_nop 1
	v_add_f32_dpp v58, v58, v58 quad_perm:[2,3,0,1] row_mask:0xf bank_mask:0xf
	v_max_f32_e32 v58, 0x3aa2425, v58
	v_rsq_f32_e32 v58, v58
	s_nop 0
	v_mul_f32_e32 v50, v49, v58
	v_mov_b32_dpp v43, v47 quad_perm:[2,0,1,3] row_mask:0xf bank_mask:0xf
	v_mov_b32_dpp v63, v47 quad_perm:[1,2,0,3] row_mask:0xf bank_mask:0xf
	v_mov_b32_dpp v62, v50 quad_perm:[2,0,1,3] row_mask:0xf bank_mask:0xf
	v_mov_b32_dpp v61, v50 quad_perm:[1,2,0,3] row_mask:0xf bank_mask:0xf
	v_mul_f32_dpp v60, v46, v43 quad_perm:[1,2,0,3] row_mask:0xf bank_mask:0xf
	v_mul_f32_dpp v51, v48, v62 quad_perm:[1,2,0,3] row_mask:0xf bank_mask:0xf
	s_nop 0
	v_fmac_f32_dpp v60, -v46, v63 quad_perm:[2,0,1,3] row_mask:0xf bank_mask:0xf
	v_fmac_f32_dpp v51, -v48, v61 quad_perm:[2,0,1,3] row_mask:0xf bank_mask:0xf
	v_mul_f32_dpp v52, v46, v48 quad_perm:[0,0,0,0] row_mask:0xf bank_mask:0xf
	v_mul_f32_dpp v53, v46, v48 quad_perm:[1,1,1,1] row_mask:0xf bank_mask:0xf
	v_mul_f32_dpp v54, v46, v48 quad_perm:[2,2,2,2] row_mask:0xf bank_mask:0xf
	v_fmac_f32_dpp v52, v47, v50 quad_perm:[0,0,0,0] row_mask:0xf bank_mask:0xf
	v_fmac_f32_dpp v53, v47, v50 quad_perm:[1,1,1,1] row_mask:0xf bank_mask:0xf
	v_fmac_f32_dpp v54, v47, v50 quad_perm:[2,2,2,2] row_mask:0xf bank_mask:0xf
	v_fmac_f32_dpp v52, v60, v51 quad_perm:[0,0,0,0] row_mask:0xf bank_mask:0xf
	v_fmac_f32_dpp v53, v60, v51 quad_perm:[1,1,1,1] row_mask:0xf bank_mask:0xf
	v_fmac_f32_dpp v54, v60, v51 quad_perm:[2,2,2,2] row_mask:0xf bank_mask:0xf
	v_mov_b32_e32 v55, 0
	v_writelane_b32 v55, s32, 48
	v_writelane_b32 v55, s33, 49
	v_writelane_b32 v55, s34, 50
	v_mul_f32_e32 v55, 0xbc800000, v55
	v_mul_f32_e32 v56, v55, v52
	v_mul_f32_e32 v57, v55, v53
	v_mul_f32_e32 v58, v55, v54
	v_add_f32_dpp v56, v56, v56 quad_perm:[1,0,3,2] row_mask:0xf bank_mask:0xf
	v_add_f32_dpp v57, v57, v57 quad_perm:[1,0,3,2] row_mask:0xf bank_mask:0xf
	v_add_f32_dpp v58, v58, v58 quad_perm:[1,0,3,2] row_mask:0xf bank_mask:0xf
	v_add_f32_dpp v56, v56, v56 quad_perm:[2,3,0,1] row_mask:0xf bank_mask:0xf
	v_add_f32_dpp v57, v57, v57 quad_perm:[2,3,0,1] row_mask:0xf bank_mask:0xf
	v_add_f32_dpp v58, v58, v58 quad_perm:[2,3,0,1] row_mask:0xf bank_mask:0xf
	v_cndmask_b32_e64 v52, v52, v56, s[26:27]
	v_cndmask_b32_e64 v53, v53, v57, s[26:27]
	v_cndmask_b32_e64 v54, v54, v58, s[26:27]
	v_subrev_u32_e32 v59, 48, v0
	v_lshlrev_b32_e32 v59, 4, v59
	s_mov_b32 s20, 0
	s_mov_b32 s21, 0xf0000
	s_mov_b64 exec, s[20:21]
	ds_write_b96 v59, v[52:54] offset:12288
	s_mov_b64 exec, -1
	s_branch .Ljoin
.Lbulk_waves:
	global_load_dwordx4 v[8:11], v1, s[4:5] offset:-2048 nt
	global_load_dwordx4 v[12:15], v1, s[4:5] offset:-1024 nt
	global_load_dwordx4 v[16:19], v1, s[4:5] offset:0 nt
	global_load_dwordx4 v[20:23], v1, s[4:5] offset:1024 nt
	global_load_dwordx4 v[24:27], v1, s[4:5] offset:2048 nt
	s_and_saveexec_b64 s[16:17], s[14:15]
	global_load_dwordx4 v[28:31], v1, s[4:5] offset:3072 nt
	s_mov_b64 exec, s[16:17]
.Ljoin:
	s_waitcnt vmcnt(3)
	ds_write_b128 v2, v[8:11]
	ds_write_b128 v2, v[12:15] offset:1024
	ds_write_b128 v2, v[16:19] offset:2048
	s_waitcnt lgkmcnt(0)
	s_barrier
	v_mov_b32_e32 v6, 0x3000
	ds_read_b96 v[32:34], v6
	ds_read_b96 v[36:38], v6 offset:16
	ds_read_b96 v[40:42], v6 offset:32
	ds_read_b96 v[44:46], v6 offset:48
	ds_read2_b32 v[48:49], v3 offset0:0 offset1:1
	ds_read_b32 v56, v3 offset:8
	ds_read2_b32 v[50:51], v3 offset0:192 offset1:193
	ds_read_b32 v57, v3 offset:776
	ds_read2_b32 v[52:53], v4 offset0:0 offset1:1
	ds_read_b32 v58, v4 offset:8
	ds_read2_b32 v[54:55], v4 offset0:192 offset1:193
	ds_read_b32 v59, v4 offset:776
	s_waitcnt lgkmcnt(6)
	v_fma_f32 v60, v48, v32, v44
	v_fma_f32 v61, v48, v33, v45
	v_fma_f32 v62, v48, v34, v46
	v_fmac_f32_e32 v60, v49, v36
	v_fmac_f32_e32 v61, v49, v37
	v_fmac_f32_e32 v62, v49, v38
	v_fmac_f32_e32 v60, v56, v40
	v_fmac_f32_e32 v61, v56, v41
	v_fmac_f32_e32 v62, v56, v42
	ds_write2_b32 v3, v60, v61 offset0:0 offset1:1
	ds_write_b32 v3, v62 offset:8
	s_waitcnt lgkmcnt(6)
	v_fma_f32 v35, v50, v32, v44
	v_fma_f32 v39, v50, v33, v45
	v_fma_f32 v43, v50, v34, v46
	v_fmac_f32_e32 v35, v51, v36
	v_fmac_f32_e32 v39, v51, v37
	v_fmac_f32_e32 v43, v51, v38
	v_fmac_f32_e32 v35, v57, v40
	v_fmac_f32_e32 v39, v57, v41
	v_fmac_f32_e32 v43, v57, v42
	ds_write2_b32 v3, v35, v39 offset0:192 offset1:193
	ds_write_b32 v3, v43 offset:776
	s_waitcnt lgkmcnt(6)
	v_fma_f32 v60, v52, v32, v44
	v_fma_f32 v61, v52, v33, v45
	v_fma_f32 v62, v52, v34, v46
	v_fmac_f32_e32 v60, v53, v36
	v_fmac_f32_e32 v61, v53, v37
	v_fmac_f32_e32 v62, v53, v38
	v_fmac_f32_e32 v60, v58, v40
	v_fmac_f32_e32 v61, v58, v41
	v_fmac_f32_e32 v62, v58, v42
	ds_write2_b32 v4, v60, v61 offset0:0 offset1:1
	ds_write_b32 v4, v62 offset:8
	s_waitcnt lgkmcnt(6)
	v_fma_f32 v35, v54, v32, v44
	v_fma_f32 v39, v54, v33, v45
	v_fma_f32 v43, v54, v34, v46
	v_fmac_f32_e32 v35, v55, v36
	v_fmac_f32_e32 v39, v55, v37
	v_fmac_f32_e32 v43, v55, v38
	v_fmac_f32_e32 v35, v59, v40
	v_fmac_f32_e32 v39, v59, v41
	v_fmac_f32_e32 v43, v59, v42
	ds_write2_b32 v4, v35, v39 offset0:192 offset1:193
	ds_write_b32 v4, v43 offset:776
	ds_read_b128 v[8:11], v2
	ds_read_b128 v[12:15], v2 offset:1024
	ds_read_b128 v[16:19], v2 offset:2048
	s_waitcnt lgkmcnt(2)
	global_store_dwordx4 v1, v[8:11], s[10:11] offset:-2048 sc0 sc1
	s_waitcnt lgkmcnt(1)
	global_store_dwordx4 v1, v[12:15], s[10:11] offset:-1024 sc0 sc1
	s_waitcnt lgkmcnt(0)
	global_store_dwordx4 v1, v[16:19], s[10:11] offset:0 sc0 sc1
	s_waitcnt vmcnt(3)
	ds_write_b128 v2, v[20:23]
	ds_write_b128 v2, v[24:27] offset:1024
	ds_write_b128 v2, v[28:31] offset:2048
	ds_read2_b32 v[48:49], v3 offset0:0 offset1:1
	ds_read_b32 v56, v3 offset:8
	ds_read2_b32 v[50:51], v3 offset0:192 offset1:193
	ds_read_b32 v57, v3 offset:776
	ds_read2_b32 v[52:53], v4 offset0:0 offset1:1
	ds_read_b32 v58, v4 offset:8
	ds_read2_b32 v[54:55], v4 offset0:192 offset1:193
	ds_read_b32 v59, v4 offset:776
	s_waitcnt lgkmcnt(6)
	v_fma_f32 v60, v48, v32, v44
	v_fma_f32 v61, v48, v33, v45
	v_fma_f32 v62, v48, v34, v46
	v_fmac_f32_e32 v60, v49, v36
	v_fmac_f32_e32 v61, v49, v37
	v_fmac_f32_e32 v62, v49, v38
	v_fmac_f32_e32 v60, v56, v40
	v_fmac_f32_e32 v61, v56, v41
	v_fmac_f32_e32 v62, v56, v42
	ds_write2_b32 v3, v60, v61 offset0:0 offset1:1
	ds_write_b32 v3, v62 offset:8
	s_waitcnt lgkmcnt(6)
	v_fma_f32 v35, v50, v32, v44
	v_fma_f32 v39, v50, v33, v45
	v_fma_f32 v43, v50, v34, v46
	v_fmac_f32_e32 v35, v51, v36
	v_fmac_f32_e32 v39, v51, v37
	v_fmac_f32_e32 v43, v51, v38
	v_fmac_f32_e32 v35, v57, v40
	v_fmac_f32_e32 v39, v57, v41
	v_fmac_f32_e32 v43, v57, v42
	ds_write2_b32 v3, v35, v39 offset0:192 offset1:193
	ds_write_b32 v3, v43 offset:776
	s_waitcnt lgkmcnt(6)
	v_fma_f32 v60, v52, v32, v44
	v_fma_f32 v61, v52, v33, v45
	v_fma_f32 v62, v52, v34, v46
	v_fmac_f32_e32 v60, v53, v36
	v_fmac_f32_e32 v61, v53, v37
	v_fmac_f32_e32 v62, v53, v38
	v_fmac_f32_e32 v60, v58, v40
	v_fmac_f32_e32 v61, v58, v41
	v_fmac_f32_e32 v62, v58, v42
	ds_write2_b32 v4, v60, v61 offset0:0 offset1:1
	ds_write_b32 v4, v62 offset:8
	s_waitcnt lgkmcnt(6)
	v_fma_f32 v35, v54, v32, v44
	v_fma_f32 v39, v54, v33, v45
	v_fma_f32 v43, v54, v34, v46
	v_fmac_f32_e32 v35, v55, v36
	v_fmac_f32_e32 v39, v55, v37
	v_fmac_f32_e32 v43, v55, v38
	v_fmac_f32_e32 v35, v59, v40
	v_fmac_f32_e32 v39, v59, v41
	v_fmac_f32_e32 v43, v59, v42
	ds_write2_b32 v4, v35, v39 offset0:192 offset1:193
	ds_write_b32 v4, v43 offset:776
	ds_read_b128 v[20:23], v2
	ds_read_b128 v[24:27], v2 offset:1024
	ds_read_b128 v[28:31], v2 offset:2048
	s_waitcnt lgkmcnt(2)
	global_store_dwordx4 v1, v[20:23], s[10:11] offset:1024 sc0 sc1
	s_waitcnt lgkmcnt(1)
	global_store_dwordx4 v1, v[24:27], s[10:11] offset:2048 sc0 sc1
	s_waitcnt lgkmcnt(0)
	s_and_saveexec_b64 s[16:17], s[14:15]
	global_store_dwordx4 v1, v[28:31], s[10:11] offset:3072 sc0 sc1
	s_endpgm

	.amdhsa_kernel _Z11align_fusedPKfS0_PKiPf
		.amdhsa_group_segment_fixed_size 12352
		.amdhsa_private_segment_fixed_size 0
		.amdhsa_kernarg_size 32
		.amdhsa_user_sgpr_count 2
		.amdhsa_user_sgpr_dispatch_ptr 0
		.amdhsa_user_sgpr_queue_ptr 0
		.amdhsa_user_sgpr_kernarg_segment_ptr 1
		.amdhsa_user_sgpr_dispatch_id 0
		.amdhsa_user_sgpr_kernarg_preload_length 0
		.amdhsa_user_sgpr_kernarg_preload_offset 0
		.amdhsa_user_sgpr_private_segment_size 0
		.amdhsa_uses_dynamic_stack 0
		.amdhsa_enable_private_segment 0
		.amdhsa_system_sgpr_workgroup_id_x 1
		.amdhsa_system_sgpr_workgroup_id_y 0
		.amdhsa_system_sgpr_workgroup_id_z 0
		.amdhsa_system_sgpr_workgroup_info 0
		.amdhsa_system_vgpr_workitem_id 0
		.amdhsa_next_free_vgpr 64
		.amdhsa_next_free_sgpr 64
		.amdhsa_accum_offset 64
		.amdhsa_reserve_vcc 1
		.amdhsa_float_round_mode_32 0
		.amdhsa_float_round_mode_16_64 0
		.amdhsa_float_denorm_mode_32 3
		.amdhsa_float_denorm_mode_16_64 3
		.amdhsa_dx10_clamp 1
		.amdhsa_ieee_mode 1
		.amdhsa_fp16_overflow 0
		.amdhsa_tg_split 0
		.amdhsa_exception_fp_ieee_invalid_op 0
		.amdhsa_exception_fp_denorm_src 0
		.amdhsa_exception_fp_ieee_div_zero 0
		.amdhsa_exception_fp_ieee_overflow 0
		.amdhsa_exception_fp_ieee_underflow 0
		.amdhsa_exception_fp_ieee_inexact 0
		.amdhsa_exception_int_div_zero 0
	.end_amdhsa_kernel

.Lfunc_end0:
	.size	_Z11align_fusedPKfS0_PKiPf, .Lfunc_end0-_Z11align_fusedPKfS0_PKiPf
	.set _Z11align_fusedPKfS0_PKiPf.num_vgpr, 64
	.set _Z11align_fusedPKfS0_PKiPf.num_agpr, 0
	.set _Z11align_fusedPKfS0_PKiPf.numbered_sgpr, 64
	.set _Z11align_fusedPKfS0_PKiPf.num_named_barrier, 0
	.set _Z11align_fusedPKfS0_PKiPf.private_seg_size, 0
	.set _Z11align_fusedPKfS0_PKiPf.uses_vcc, 1
	.set _Z11align_fusedPKfS0_PKiPf.uses_flat_scratch, 0
	.set _Z11align_fusedPKfS0_PKiPf.has_dyn_sized_stack, 0
	.set _Z11align_fusedPKfS0_PKiPf.has_recursion, 0
	.set _Z11align_fusedPKfS0_PKiPf.has_indirect_call, 0

amdhsa.kernels:
  - .agpr_count:     0
    .args:
      - .actual_access:  read_only
        .address_space:  global
        .offset:         0
        .size:           8
        .value_kind:     global_buffer
      - .actual_access:  read_only
        .address_space:  global
        .offset:         8
        .size:           8
        .value_kind:     global_buffer
      - .actual_access:  read_only
        .address_space:  global
        .offset:         16
        .size:           8
        .value_kind:     global_buffer
      - .actual_access:  write_only
        .address_space:  global
        .offset:         24
        .size:           8
        .value_kind:     global_buffer
    .group_segment_fixed_size: 12352
    .kernarg_segment_align: 8
    .kernarg_segment_size: 32
    .language:       OpenCL C
    .language_version:
      - 2
      - 0
    .max_flat_workgroup_size: 256
    .name:           _Z11align_fusedPKfS0_PKiPf
    .private_segment_fixed_size: 0
    .sgpr_count:     70
    .sgpr_spill_count: 0
    .symbol:         _Z11align_fusedPKfS0_PKiPf.kd
    .uniform_work_group_size: 1
    .uses_dynamic_stack: false
    .vgpr_count:     64
    .vgpr_spill_count: 0
    .wavefront_size: 64
